# P15 split at 4 full rounds: tail units run in a second pass while other WGs already combine+normalize rows not touching the tail expert; remaining rows after a second grid barrier
# baseline (speedup 1.0000x reference)
; #define LAS __attribute__((address_space(3)))
; __device__ __forceinline__ int tid_opaque() { int t = threadIdx.x; asm volatile("" : "+v"(t)); return t; }
; #define MKCTX() const Ctx P{InTbl{in_tbl()}, (float*)*(__attribute__((address_space(1))) float* const*)((const char*)in_tbl() + offsetof(Params, out)), ws}
; #define IN(k) (((PH_MASK >> (k)) & 1) && KARG_I(ph_lo) <= (k) && (k) < KARG_I(ph_hi))
; __device__ __forceinline__ void moe_tables(const Ctx& P, volatile LAS int* tab, int nN) {
;     if (tid_opaque() == 0) { const unsigned* ecnt = (const unsigned*)(P.ws + WS_CTL) + CW_ECNT; int pb = 0, cu = 0;
;         for (int e = 0; e < 8; ++e) { const int c = (int)ecnt[64 * e], np = (c + 255) >> 8; tab[e] = c; tab[8 + e] = pb; tab[16 + e] = cu; pb += np; cu += np * nN; }
;         tab[24] = cu; }
;     __syncthreads();
; }
; __global__ void __launch_bounds__(512, 2) fwd_kernel(Params KP) {
;     ...
;     if (IN(15)) { MKCTX();
;         moe_tables(P, tab, 8);
;         pg8::MoeSched S{(const char*)(ws + WS_WM2), (const int*)(ws + WS_LIST), tab, DFFE / 2, DFFE / 2, G, bx, 8, 0, (size_t)DM * DFFE, DFFE / 128};
.LBB0_2615:
	s_or_b64 exec, exec, s[40:41]
	s_mov_b32 s99, 0
	s_load_dword s100, s[0:1], 0x12c
	s_lshl_b32 s101, s39, 2
	s_waitcnt lgkmcnt(0)
	s_cmp_gt_i32 s100, 16
	s_cselect_b32 s101, s101, 0x7fffffff
.Lp15_reenter:
	s_mov_b64 s[2:3], s[0:1]
	s_nop 0
	v_mov_b64_e32 v[2:3], s[2:3]
	flat_load_dword v1, v[2:3] offset:296
	s_waitcnt vmcnt(0) lgkmcnt(0)
	v_cmp_gt_i32_e32 vcc, 16, v1
	s_and_saveexec_b64 s[10:11], vcc
	s_cbranch_execz .LBB0_2648
	s_mov_b64 s[2:3], s[0:1]
	s_nop 0
	v_mov_b64_e32 v[2:3], s[2:3]
	flat_load_dword v1, v[2:3] offset:300
	s_waitcnt vmcnt(0) lgkmcnt(0)
	v_cmp_lt_i32_e32 vcc, 15, v1
	s_and_b64 exec, exec, vcc
	s_cbranch_execz .LBB0_2648
	s_cmp_eq_u32 s99, 0
	s_cselect_b32 s99, 1, s99
	s_mov_b64 s[2:3], s[0:1]
	s_mov_b64 s[2:3], s[0:1]
	v_mov_b32_e32 v1, v0
	s_nop 0
	v_cmp_eq_u32_e32 vcc, 0, v1
	s_and_saveexec_b64 s[2:3], vcc
	s_cbranch_execz .LBB0_2619
	s_cmp_eq_u32 s99, 2
	s_cbranch_scc1 .Lp15_tabfix
	v_mov_b32_e32 v1, 0x4000
	global_load_dword v2, v1, s[36:37]
	s_add_i32 s4, 0, 0x20100
	s_add_i32 s5, 0, 0x20120
	s_add_i32 s6, 0, 0x20140
	v_mov_b32_e32 v4, s4
	v_mov_b32_e32 v3, 0
	v_mov_b32_e32 v5, s5
	v_mov_b32_e32 v6, s6
	s_add_i32 s4, 0, 0x20104
	s_add_i32 s5, 0, 0x20124
	s_add_i32 s6, 0, 0x20144
	s_add_i32 s7, 0, 0x20160
	s_waitcnt vmcnt(0)
	ds_write_b32 v4, v2
	ds_write_b32 v5, v3
	ds_write_b32 v6, v3
	global_load_dword v3, v1, s[36:37] offset:256
	v_add_u32_e32 v2, 0xff, v2
	v_mov_b32_e32 v4, s4
	v_ashrrev_i32_e32 v2, 8, v2
	v_mov_b32_e32 v5, s5
	v_mov_b32_e32 v6, s6
	v_lshlrev_b32_e32 v7, 3, v2
	s_add_i32 s4, 0, 0x20108
	s_add_i32 s5, 0, 0x20128
	s_add_i32 s6, 0, 0x20148
	s_waitcnt vmcnt(0)
	ds_write_b32 v4, v3
	ds_write_b32 v5, v2
	ds_write_b32 v6, v7
	global_load_dword v4, v1, s[36:37] offset:512
	v_add_u32_e32 v3, 0xff, v3
	v_ashrrev_i32_e32 v3, 8, v3
	v_mov_b32_e32 v5, s4
	v_add_u32_e32 v2, v3, v2
	v_mov_b32_e32 v6, s5
	v_mov_b32_e32 v7, s6
	v_lshlrev_b32_e32 v3, 3, v2
	s_add_i32 s4, 0, 0x2010c
	s_add_i32 s5, 0, 0x2012c
	s_add_i32 s6, 0, 0x2014c
	s_waitcnt vmcnt(0)
	ds_write_b32 v5, v4
	ds_write_b32 v6, v2
	ds_write_b32 v7, v3
	global_load_dword v3, v1, s[36:37] offset:768
	v_add_u32_e32 v4, 0xff, v4
	v_ashrrev_i32_e32 v4, 8, v4
	v_mov_b32_e32 v5, s4
	v_add_u32_e32 v2, v4, v2
	v_mov_b32_e32 v6, s5
	v_mov_b32_e32 v7, s6
	v_lshlrev_b32_e32 v4, 3, v2
	s_add_i32 s4, 0, 0x20110
	s_add_i32 s5, 0, 0x20130
	s_add_i32 s6, 0, 0x20150
	s_waitcnt vmcnt(0)
	ds_write_b32 v5, v3
	ds_write_b32 v6, v2
	ds_write_b32 v7, v4
	global_load_dword v4, v1, s[36:37] offset:1024
	v_add_u32_e32 v3, 0xff, v3
	v_ashrrev_i32_e32 v3, 8, v3
	v_mov_b32_e32 v5, s4
	v_add_u32_e32 v2, v3, v2
	v_mov_b32_e32 v6, s5
	v_mov_b32_e32 v7, s6
	v_lshlrev_b32_e32 v3, 3, v2
	s_add_i32 s4, 0, 0x20114
	s_add_i32 s5, 0, 0x20134
	s_add_i32 s6, 0, 0x20154
	s_waitcnt vmcnt(0)
	ds_write_b32 v5, v4
	ds_write_b32 v6, v2
	ds_write_b32 v7, v3
	global_load_dword v3, v1, s[36:37] offset:1280
	v_add_u32_e32 v4, 0xff, v4
	v_ashrrev_i32_e32 v4, 8, v4
	v_mov_b32_e32 v5, s4
	v_add_u32_e32 v2, v4, v2
	v_mov_b32_e32 v6, s5
	v_mov_b32_e32 v7, s6
	v_lshlrev_b32_e32 v4, 3, v2
	s_add_i32 s4, 0, 0x20118
	s_add_i32 s5, 0, 0x20138
	s_add_i32 s6, 0, 0x20158
	s_waitcnt vmcnt(0)
	ds_write_b32 v5, v3
	ds_write_b32 v6, v2
	ds_write_b32 v7, v4
	global_load_dword v4, v1, s[36:37] offset:1536
	v_add_u32_e32 v3, 0xff, v3
	v_ashrrev_i32_e32 v3, 8, v3
	v_mov_b32_e32 v5, s4
	v_add_u32_e32 v2, v3, v2
	v_mov_b32_e32 v6, s5
	v_mov_b32_e32 v7, s6
	v_lshlrev_b32_e32 v3, 3, v2
	s_add_i32 s4, 0, 0x2011c
	s_add_i32 s5, 0, 0x2013c
	s_add_i32 s6, 0, 0x2015c
	s_waitcnt vmcnt(0)
	ds_write_b32 v5, v4
	ds_write_b32 v6, v2
	ds_write_b32 v7, v3
	global_load_dword v1, v1, s[36:37] offset:1792
	v_add_u32_e32 v4, 0xff, v4
	v_ashrrev_i32_e32 v4, 8, v4
	v_mov_b32_e32 v3, s4
	v_add_u32_e32 v2, v4, v2
	v_mov_b32_e32 v5, s5
	v_mov_b32_e32 v6, s6
	v_lshlrev_b32_e32 v4, 3, v2
	s_waitcnt vmcnt(0)
	ds_write_b32 v3, v1
	ds_write_b32 v5, v2
	ds_write_b32 v6, v4
	v_add_u32_e32 v7, 0xff, v1
	v_ashrrev_i32_e32 v1, 8, v7
	v_add_u32_e32 v1, v1, v2
	v_lshlrev_b32_e32 v1, 3, v1
	v_mov_b32_e32 v2, s7
	v_mov_b32_e32 v3, 0x20170
	ds_write_b32 v3, v1
	v_min_i32_e32 v1, s101, v1
	ds_write_b32 v2, v1
	s_branch .LBB0_2619
.Lp15_tabfix:
	v_mov_b32_e32 v1, 0x20170
	ds_read_b32 v1, v1
	v_mov_b32_e32 v2, 0x20160
	s_waitcnt lgkmcnt(0)
	ds_write_b32 v2, v1

; #define MKCTX() const Ctx P{InTbl{in_tbl()}, (float*)*(__attribute__((address_space(1))) float* const*)((const char*)in_tbl() + offsetof(Params, out)), ws}
; #define IN(k) (((PH_MASK >> (k)) & 1) && KARG_I(ph_lo) <= (k) && (k) < KARG_I(ph_hi))
; #define SEAM(k) do { if (IN(k) && IN((k) + 1)) { XcdBarrier bar_; bar_.bar = (unsigned*)(ws + WS_CTL) + CW_BAR; bar_.x = xb_xcc_id(); bar_.st = MISC + 8; bar_.G = (unsigned)KARG_I(grid); xcd_barrier(bar_); } } while (0)
; __device__ __forceinline__ void xcd_barrier(const XcdBarrier& b) {
;     asm volatile("s_waitcnt vmcnt(0)" ::: "memory");
;     __syncthreads();
;     int t_ = threadIdx.x; asm volatile("" : "+v"(t_));
;     if (t_ == 0) {
;         unsigned* bar = b.bar;
;         __builtin_amdgcn_s_waitcnt(0);
;         unsigned nloc = b.st[0], nx = b.st[1];
;         if (nloc == 0u) { xcd_barrier_complete(bar, b.x, b.G, nloc, nx); b.st[0] = nloc; b.st[1] = nx; }
; __global__ void __launch_bounds__(512, 2) fwd_kernel(Params KP) {
;     ...
;     } SEAM(15);
;     if (IN(16)) { MKCTX(); moe_tables(P, tab, 8); phase_final(P, tab, vcu, G); }
.LBB0_2648:
	s_or_b64 exec, exec, s[10:11]
	s_cmp_eq_u32 s99, 1
	s_cselect_b32 s98, s8, s98
	s_cmp_eq_u32 s99, 2
	s_cbranch_scc0 .Lseam15
	s_mov_b64 s[90:91], s[0:1]
	v_mov_b32_e32 v203, v0
	s_branch .Lp16_body
.Lseam15:
	s_mov_b64 s[2:3], s[0:1]
	s_nop 0
	v_mov_b64_e32 v[2:3], s[2:3]
	flat_load_dword v1, v[2:3] offset:296
	s_waitcnt vmcnt(0) lgkmcnt(0)
	v_cmp_gt_i32_e32 vcc, 16, v1
	s_and_saveexec_b64 s[34:35], vcc
	s_cbranch_execz .LBB0_2706
	s_mov_b64 s[2:3], s[0:1]
	s_nop 0
	v_mov_b64_e32 v[2:3], s[2:3]
	flat_load_dword v1, v[2:3] offset:300
	s_waitcnt vmcnt(0) lgkmcnt(0)
	v_cmp_lt_i32_e32 vcc, 15, v1
	s_and_b64 exec, exec, vcc
	s_cbranch_execz .LBB0_2706
	s_mov_b64 s[2:3], s[0:1]
	s_nop 0
	v_mov_b64_e32 v[2:3], s[2:3]
	flat_load_dword v1, v[2:3] offset:296
	s_waitcnt vmcnt(0) lgkmcnt(0)
	v_cmp_gt_i32_e32 vcc, 17, v1
	s_and_b64 exec, exec, vcc
	s_cbranch_execz .LBB0_2706
	s_mov_b64 s[2:3], s[0:1]
	s_nop 0
	v_mov_b64_e32 v[2:3], s[2:3]
	flat_load_dword v1, v[2:3] offset:300
	s_waitcnt vmcnt(0) lgkmcnt(0)
	v_cmp_lt_i32_e32 vcc, 16, v1
	s_and_b64 exec, exec, vcc
	s_cbranch_execz .LBB0_2706
	s_mov_b64 s[4:5], s[0:1]
	s_getreg_b32 s2, hwreg(HW_REG_XCC_ID, 0, 4)
	v_mov_b32_e32 v1, v0
	v_mov_b64_e32 v[2:3], s[4:5]
	flat_load_dword v17, v[2:3] offset:308
	s_waitcnt vmcnt(0)
	s_waitcnt lgkmcnt(0)
	s_barrier
	s_nop 0
	v_cmp_eq_u32_e32 vcc, 0, v1
	s_and_b64 exec, exec, vcc
	s_cbranch_execz .LBB0_2705
	s_add_i32 s3, 0, 0x20020
	v_mov_b32_e32 v1, s3
	s_waitcnt vmcnt(0) expcnt(0) lgkmcnt(0)
	ds_read_b32 v4, v1
	s_add_i32 s3, 0, 0x20024
	v_mov_b32_e32 v1, s3
	ds_read_b32 v2, v1
	s_and_b32 s38, s2, 15
	s_waitcnt lgkmcnt(1)
	v_cmp_ne_u32_e32 vcc, 0, v4
	s_cbranch_vccnz .LBB0_2669
	s_add_u32 s2, s36, 0x1000
	s_addc_u32 s3, s37, 0
	s_add_u32 s4, s36, 0x1100
	s_addc_u32 s5, s37, 0
	s_add_u32 s6, s36, 0x1200
	s_addc_u32 s7, s37, 0
	s_add_u32 s8, s36, 0x1300
	s_addc_u32 s9, s37, 0
	s_mov_b32 s26, 1
	s_mov_b64 s[10:11], 0
	v_mov_b32_e32 v18, 0
	s_branch .LBB0_2657

; #define LAS __attribute__((address_space(3)))
; __device__ __forceinline__ int tid_opaque() { int t = threadIdx.x; asm volatile("" : "+v"(t)); return t; }
; #define MKCTX() const Ctx P{InTbl{in_tbl()}, (float*)*(__attribute__((address_space(1))) float* const*)((const char*)in_tbl() + offsetof(Params, out)), ws}
; #define IN(k) (((PH_MASK >> (k)) & 1) && KARG_I(ph_lo) <= (k) && (k) < KARG_I(ph_hi))
; __device__ __forceinline__ void moe_tables(const Ctx& P, volatile LAS int* tab, int nN) {
;     if (tid_opaque() == 0) { const unsigned* ecnt = (const unsigned*)(P.ws + WS_CTL) + CW_ECNT; int pb = 0, cu = 0;
;         for (int e = 0; e < 8; ++e) { const int c = (int)ecnt[64 * e], np = (c + 255) >> 8; tab[e] = c; tab[8 + e] = pb; tab[16 + e] = cu; pb += np; cu += np * nN; }
;         tab[24] = cu; }
;     __syncthreads();
; }
; __global__ void __launch_bounds__(512, 2) fwd_kernel(Params KP) {
;     ...
;     if (IN(16)) { MKCTX(); moe_tables(P, tab, 8); phase_final(P, tab, vcu, G); }
.LBB0_2706:
	s_or_b64 exec, exec, s[34:35]
	s_mov_b64 s[2:3], s[0:1]
	s_nop 0
	v_mov_b64_e32 v[2:3], s[2:3]
	flat_load_dword v1, v[2:3] offset:296
	s_waitcnt vmcnt(0) lgkmcnt(0)
	v_cmp_gt_i32_e32 vcc, 17, v1
	s_and_saveexec_b64 s[2:3], vcc
	s_cbranch_execz .LBB0_2713
	s_mov_b64 s[2:3], s[0:1]
	s_nop 0
	v_mov_b64_e32 v[2:3], s[2:3]
	flat_load_dword v1, v[2:3] offset:300
	s_waitcnt vmcnt(0) lgkmcnt(0)
	v_cmp_lt_i32_e32 vcc, 16, v1
	s_and_b64 exec, exec, vcc
	s_cbranch_execz .LBB0_2713
	s_cmp_eq_u32 s99, 1
	s_cbranch_scc0 .Lp16_body
	s_mov_b32 s99, 2
	s_lshl_b32 s101, s39, 2
	s_add_i32 s8, s98, s101
	s_mov_b32 s101, 0x7fffffff
	s_branch .Lp15_reenter
.Lp16_body:
	s_mov_b64 s[8:9], s[0:1]
	v_mov_b32_e32 v1, v0
	v_mov_b64_e32 v[2:3], s[0:1]
	flat_load_dwordx2 v[2:3], v[2:3] offset:280
	s_nop 0
	s_cmp_ge_u32 s99, 2
	s_cbranch_scc1 .Lp16_tabok
	v_cmp_eq_u32_e32 vcc, 0, v1
	s_and_saveexec_b64 s[0:1], vcc
	s_cbranch_execz .LBB0_2710
	v_mov_b32_e32 v1, 0x4000
	global_load_dword v4, v1, s[36:37]
	s_add_i32 s2, 0, 0x20100
	s_add_i32 s3, 0, 0x20120
	s_add_i32 s4, 0, 0x20140
	v_mov_b32_e32 v6, s2
	v_mov_b32_e32 v5, 0
	v_mov_b32_e32 v7, s3
	v_mov_b32_e32 v8, s4
	s_add_i32 s2, 0, 0x20104
	s_add_i32 s3, 0, 0x20124
	s_add_i32 s4, 0, 0x20144
	s_add_i32 s5, 0, 0x20160
	s_waitcnt vmcnt(0)
	ds_write_b32 v6, v4
	ds_write_b32 v7, v5
	ds_write_b32 v8, v5
	global_load_dword v5, v1, s[36:37] offset:256
	v_add_u32_e32 v4, 0xff, v4
	v_mov_b32_e32 v6, s2
	v_ashrrev_i32_e32 v4, 8, v4
	v_mov_b32_e32 v7, s3
	v_mov_b32_e32 v8, s4
	v_lshlrev_b32_e32 v9, 3, v4
	s_add_i32 s2, 0, 0x20108
	s_add_i32 s3, 0, 0x20128
	s_add_i32 s4, 0, 0x20148
	s_waitcnt vmcnt(0)
	ds_write_b32 v6, v5
	ds_write_b32 v7, v4
	ds_write_b32 v8, v9
	global_load_dword v6, v1, s[36:37] offset:512
	v_add_u32_e32 v5, 0xff, v5
	v_ashrrev_i32_e32 v5, 8, v5
	v_mov_b32_e32 v7, s2
	v_add_u32_e32 v4, v5, v4
	v_mov_b32_e32 v8, s3
	v_mov_b32_e32 v9, s4
	v_lshlrev_b32_e32 v5, 3, v4
	s_add_i32 s2, 0, 0x2010c
	s_add_i32 s3, 0, 0x2012c
	s_add_i32 s4, 0, 0x2014c
	s_waitcnt vmcnt(0)
	ds_write_b32 v7, v6
	ds_write_b32 v8, v4
	ds_write_b32 v9, v5
	global_load_dword v5, v1, s[36:37] offset:768
	v_add_u32_e32 v6, 0xff, v6
	v_ashrrev_i32_e32 v6, 8, v6
	v_mov_b32_e32 v7, s2
	v_add_u32_e32 v4, v6, v4
	v_mov_b32_e32 v8, s3
	v_mov_b32_e32 v9, s4
	v_lshlrev_b32_e32 v6, 3, v4
	s_add_i32 s2, 0, 0x20110
	s_add_i32 s3, 0, 0x20130
	s_add_i32 s4, 0, 0x20150
	s_waitcnt vmcnt(0)
	ds_write_b32 v7, v5
	ds_write_b32 v8, v4
	ds_write_b32 v9, v6
	global_load_dword v6, v1, s[36:37] offset:1024
	v_add_u32_e32 v5, 0xff, v5
	v_ashrrev_i32_e32 v5, 8, v5
	v_mov_b32_e32 v7, s2
	v_add_u32_e32 v4, v5, v4
	v_mov_b32_e32 v8, s3
	v_mov_b32_e32 v9, s4
	v_lshlrev_b32_e32 v5, 3, v4
	s_add_i32 s2, 0, 0x20114
	s_add_i32 s3, 0, 0x20134
	s_add_i32 s4, 0, 0x20154
	s_waitcnt vmcnt(0)
	ds_write_b32 v7, v6
	ds_write_b32 v8, v4
	ds_write_b32 v9, v5
	global_load_dword v5, v1, s[36:37] offset:1280
	v_add_u32_e32 v6, 0xff, v6
	v_ashrrev_i32_e32 v6, 8, v6
	v_mov_b32_e32 v7, s2
	v_add_u32_e32 v4, v6, v4
	v_mov_b32_e32 v8, s3
	v_mov_b32_e32 v9, s4
	v_lshlrev_b32_e32 v6, 3, v4
	s_add_i32 s2, 0, 0x20118
	s_add_i32 s3, 0, 0x20138
	s_add_i32 s4, 0, 0x20158
	s_waitcnt vmcnt(0)
	ds_write_b32 v7, v5
	ds_write_b32 v8, v4
	ds_write_b32 v9, v6
	global_load_dword v6, v1, s[36:37] offset:1536
	v_add_u32_e32 v5, 0xff, v5
	v_ashrrev_i32_e32 v5, 8, v5
	v_mov_b32_e32 v7, s2
	v_add_u32_e32 v4, v5, v4
	v_mov_b32_e32 v8, s3
	v_mov_b32_e32 v9, s4
	v_lshlrev_b32_e32 v5, 3, v4
	s_add_i32 s2, 0, 0x2011c
	s_add_i32 s3, 0, 0x2013c
	s_add_i32 s4, 0, 0x2015c
	s_waitcnt vmcnt(0)
	ds_write_b32 v7, v6
	ds_write_b32 v8, v4
	ds_write_b32 v9, v5
	global_load_dword v1, v1, s[36:37] offset:1792
	v_add_u32_e32 v6, 0xff, v6
	v_ashrrev_i32_e32 v6, 8, v6
	v_mov_b32_e32 v5, s2
	v_add_u32_e32 v4, v6, v4
	v_mov_b32_e32 v7, s3
	v_mov_b32_e32 v8, s4
	v_lshlrev_b32_e32 v6, 3, v4
	s_waitcnt vmcnt(0)
	ds_write_b32 v5, v1
	ds_write_b32 v7, v4
	ds_write_b32 v8, v6
	v_add_u32_e32 v9, 0xff, v1
	v_ashrrev_i32_e32 v1, 8, v9
	v_add_u32_e32 v1, v1, v4
	v_lshlrev_b32_e32 v1, 3, v1
	v_mov_b32_e32 v4, s5
	ds_write_b32 v4, v1

; #define LAS __attribute__((address_space(3)))
; __device__ __forceinline__ void phase_final(const Ctx& P, volatile LAS int* tab, int vcu, int G) {
;     const int tid = threadIdx.x, lane = tid & 63, wave = __builtin_amdgcn_readfirstlane(tid >> 6);
;     const int gw = vcu * 8 + wave, NGW = G * 8;
;     const float* mod = (const float*)(P.ws + WS_MOD) + (size_t)5 * NMOD; const int* tok = (const int*)(P.ws + WS_TOK); const bf16_t* YB = (const bf16_t*)(P.ws + WS_YB);
;     for (int row = gw; row < ML; row += NGW) {
;         const int e1 = tok[row * 8], pos1 = tok[row * 8 + 1], e2 = tok[row * 8 + 2], pos2 = tok[row * 8 + 3]; const float p1 = ((const float*)tok)[row * 8 + 4], p2 = ((const float*)tok)[row * 8 + 5];
;         const bf16_t* y1 = YB + (size_t)(tab[8 + e1] * 256 + pos1) * DM; const bf16_t* y2 = YB + (size_t)(tab[8 + e2] * 256 + pos2) * DM;
;         const bf16_t* xr = (const bf16_t*)(P.ws + WS_XA) + (size_t)row * DM; const float* g2 = mod + (size_t)(row >> 12) * NMOD + 5 * DM;
.Lp16_tabok:
	v_readfirstlane_b32 s0, v0
	s_lshr_b32 s1, s0, 6
	s_lshl_b32 s3, s33, 3
	s_add_i32 s10, s1, s3
	s_cmpk_gt_i32 s10, 0x3fff
	s_waitcnt lgkmcnt(0)
	s_barrier
	s_cbranch_scc1 .LBB0_2713
	v_and_b32_e32 v201, 7, v0
	v_lshlrev_b32_e32 v201, 2, v201
	v_add_u32_e32 v201, 0x20144, v201
	ds_read_b32 v202, v201
	s_lshl_b32 s16, s39, 2
	s_mov_b32 s20, 0
	s_mov_b32 s21, 0x7fffffff
	s_waitcnt lgkmcnt(0)
	v_cmp_ge_u32_e32 vcc, s16, v202
	s_nop 1
	s_and_b32 s17, vcc_lo, 0xff
	s_bcnt1_i32_b32 s22, s17
	v_readlane_b32 s18, v202, 7
	s_cmp_eq_u32 s99, 0
	s_cbranch_scc1 .Lp16_bounds_done
	s_add_i32 s19, s98, s16
	s_cmp_lt_i32 s19, s18
	s_cselect_b32 s19, 1, 0
	s_cmp_eq_u32 s99, 2
	s_cbranch_scc0 .Lp16_modeB
	s_cmp_eq_u32 s19, 1
	s_cbranch_scc1 .LBB0_2713
	s_mov_b32 s21, s22
	s_branch .Lp16_bounds_done
.Lp16_modeB:
	s_cmp_eq_u32 s19, 1
	s_cbranch_scc1 .Lp16_bounds_done
	s_mov_b32 s20, s22
.Lp16_bounds_done:
	v_lshlrev_b32_e32 v1, 2, v0
	v_and_b32_e32 v4, 0xfc, v1
	v_mbcnt_lo_u32_b32 v1, -1, 0
	v_mbcnt_hi_u32_b32 v1, -1, v1
	v_and_b32_e32 v5, 64, v1
	v_add_u32_e32 v5, 64, v5
	v_xor_b32_e32 v6, 1, v1
	v_cmp_lt_i32_e32 vcc, v6, v5
	s_lshl_b32 s0, s39, 3
	v_mov_b32_e32 v29, 0
	v_cndmask_b32_e32 v6, v1, v6, vcc
	v_lshlrev_b32_e32 v58, 2, v6
	v_xor_b32_e32 v6, 2, v1
	v_cmp_lt_i32_e32 vcc, v6, v5
	v_lshlrev_b32_e32 v28, 1, v4
	s_add_u32 s11, s36, 0x200000
	v_cndmask_b32_e32 v6, v1, v6, vcc
	v_lshlrev_b32_e32 v59, 2, v6
	v_xor_b32_e32 v6, 4, v1
	v_cmp_lt_i32_e32 vcc, v6, v5
	v_lshl_add_u64 v[20:21], s[36:37], 0, v[28:29]
	s_mov_b64 s[4:5], 0x24ac0000
	v_cndmask_b32_e32 v6, v1, v6, vcc
	v_lshlrev_b32_e32 v60, 2, v6
	v_xor_b32_e32 v6, 8, v1
	v_cmp_lt_i32_e32 vcc, v6, v5
	s_addc_u32 s12, s37, 0
	v_lshl_add_u64 v[30:31], v[20:21], 0, s[4:5]
	v_cndmask_b32_e32 v6, v1, v6, vcc
	v_lshlrev_b32_e32 v61, 2, v6
	v_xor_b32_e32 v6, 16, v1
	v_cmp_lt_i32_e32 vcc, v6, v5
	s_lshl_b32 s2, s33, 6
	s_lshl_b32 s4, s1, 3
	v_cndmask_b32_e32 v6, v1, v6, vcc
	s_add_i32 s2, s2, s4
	s_lshl_b32 s13, s39, 6
	s_ashr_i32 s4, s3, 31
	v_lshlrev_b32_e32 v62, 2, v6
	v_xor_b32_e32 v6, 32, v1
	s_add_u32 s6, s1, s3
	v_cmp_lt_i32_e32 vcc, v6, v5
	s_addc_u32 s7, 0, s4
	s_lshl_b64 s[4:5], s[6:7], 13
	v_cndmask_b32_e32 v1, v1, v6, vcc
	v_and_b32_e32 v5, 63, v0
	v_lshlrev_b32_e32 v63, 2, v1
	v_lshl_or_b32 v0, v5, 4, s4
	v_mov_b32_e32 v1, s5
	s_waitcnt vmcnt(0)
	v_lshl_add_u64 v[0:1], v[2:3], 0, v[0:1]
	s_mov_b64 s[4:5], 0x1000
	s_ashr_i32 s1, s0, 31
	v_lshl_add_u64 v[32:33], v[0:1], 0, s[4:5]
	s_lshl_b64 s[4:5], s[0:1], 13
	s_lshl_b64 s[6:7], s[6:7], 12
	s_add_u32 s6, s36, s6
	v_lshlrev_b32_e32 v28, 3, v5
	s_addc_u32 s7, s37, s7
	v_or_b32_e32 v6, 0x100, v4
	v_or_b32_e32 v8, 0x200, v4
	v_or_b32_e32 v10, 0x300, v4
	v_or_b32_e32 v12, 0x400, v4
	v_or_b32_e32 v14, 0x500, v4
	v_or_b32_e32 v16, 0x600, v4
	v_or_b32_e32 v18, 0x700, v4
	v_lshl_add_u64 v[0:1], s[6:7], 0, v[28:29]
	s_mov_b64 s[6:7], 0x1c2c0800
	v_lshl_add_u64 v[34:35], v[0:1], 0, s[6:7]
	s_lshl_b64 s[6:7], s[0:1], 12
	s_add_i32 s1, 0, 0x20100
	v_lshlrev_b32_e32 v28, 2, v4
	v_lshlrev_b32_e32 v64, 2, v6
	v_lshlrev_b32_e32 v65, 2, v8
	v_lshlrev_b32_e32 v66, 2, v10
	v_lshlrev_b32_e32 v36, 2, v12
	v_mov_b32_e32 v37, v29
	v_lshlrev_b32_e32 v38, 2, v14
	v_mov_b32_e32 v39, v29
	v_lshlrev_b32_e32 v40, 2, v16
	v_mov_b32_e32 v41, v29
	v_lshlrev_b32_e32 v42, 2, v18
	v_mov_b32_e32 v43, v29
	v_mov_b32_e32 v67, 0x358637bd
	v_mov_b64_e32 v[44:45], s[8:9]
	flat_load_dwordx2 v[82:83], v[44:45] offset:272
	s_ashr_i32 s3, s2, 31
	s_lshl_b64 s[8:9], s[2:3], 2
	s_add_u32 s8, s11, s8
	s_addc_u32 s9, s12, s9
	global_load_dwordx4 v[194:197], v29, s[8:9]
	global_load_dwordx2 v[198:199], v29, s[8:9] offset:16
	s_mov_b64 s[14:15], 0x1000
	s_waitcnt vmcnt(2) lgkmcnt(0)
	v_lshl_add_u64 v[82:83], v[82:83], 0, v[28:29]
	v_lshl_add_u64 v[84:85], v[82:83], 0, s[14:15]
	global_load_dwordx4 v[162:165], v[82:83], off
	global_load_dwordx4 v[166:169], v[82:83], off offset:1024
	global_load_dwordx4 v[170:173], v[82:83], off offset:2048
	global_load_dwordx4 v[174:177], v[82:83], off offset:3072
	global_load_dwordx4 v[178:181], v[84:85], off
	global_load_dwordx4 v[182:185], v[84:85], off offset:1024
	global_load_dwordx4 v[186:189], v[84:85], off offset:2048
	global_load_dwordx4 v[190:193], v[84:85], off offset:3072
	s_waitcnt vmcnt(0)
; __device__ __forceinline__ float bf_lo(unsigned w) { return __uint_as_float(w << 16); }
; __device__ __forceinline__ float bf_hi(unsigned w) { return __uint_as_float(w & 0xffff0000u); }
; __device__ __forceinline__ f32x4 ld4_bf(const bf16_t* p) { const u32x2 w = *(const u32x2*)p; return (f32x4){bf_lo(w.x), bf_hi(w.x), bf_lo(w.y), bf_hi(w.y)}; }
; __device__ __forceinline__ float sq4(const f32x4 v) { return (v[0] * v[0] + v[1] * v[1]) + (v[2] * v[2] + v[3] * v[3]); }
; __device__ __forceinline__ void phase_final(const Ctx& P, volatile LAS int* tab, int vcu, int G) {
;     ...
;     for (int row = gw; row < ML; row += NGW) {
;         const int e1 = tok[row * 8], pos1 = tok[row * 8 + 1], e2 = tok[row * 8 + 2], pos2 = tok[row * 8 + 3]; const float p1 = ((const float*)tok)[row * 8 + 4], p2 = ((const float*)tok)[row * 8 + 5];
;         const bf16_t* y1 = YB + (size_t)(tab[8 + e1] * 256 + pos1) * DM; const bf16_t* y2 = YB + (size_t)(tab[8 + e2] * 256 + pos2) * DM;
;         const bf16_t* xr = (const bf16_t*)(P.ws + WS_XA) + (size_t)row * DM; const float* g2 = mod + (size_t)(row >> 12) * NMOD + 5 * DM;
;         f32x4 v[8]; float ss = 0.f;
; #pragma unroll
;         for (int j = 0; j < 8; ++j) { const int c = 4 * lane + 256 * j; const f32x4 x4 = ld4_bf(xr + c), g4 = *(const f32x4*)(g2 + c); const u32x2 a = *(const u32x2*)(y1 + c), b = *(const u32x2*)(y2 + c);
;             const f32x4 ya = (f32x4){bf_lo(a.x), bf_hi(a.x), bf_lo(a.y), bf_hi(a.y)}, yb = (f32x4){bf_lo(b.x), bf_hi(b.x), bf_lo(b.y), bf_hi(b.y)};
;             v[j] = x4 + g4 * (ya * p1 + yb * p2); ss += sq4(v[j]); }
.LBB0_2712:
	v_mov_b32_e32 v16, v194
	v_mov_b32_e32 v17, v195
	v_mov_b32_e32 v18, v196
	v_mov_b32_e32 v19, v197
	v_mov_b32_e32 v46, v198
	v_mov_b32_e32 v47, v199
	v_max_i32_e32 v200, v194, v196
	s_ashr_i32 s3, s10, 12
	s_mul_hi_i32 s8, s3, 0xc000
	s_mul_i32 s3, s3, 0xc000
	s_add_u32 s3, s36, s3
	s_addc_u32 s9, s37, s8
	s_add_u32 s8, s3, 0x146000
	s_addc_u32 s9, s9, 0
	s_add_i32 s10, s10, s0
	s_add_i32 s2, s2, s13
	s_ashr_i32 s3, s2, 31
	s_lshl_b64 s[14:15], s[2:3], 2
	s_add_u32 s14, s11, s14
	s_addc_u32 s15, s12, s15
	s_cmpk_lt_i32 s10, 0x4000
	s_cselect_b32 s17, 1, 0
	v_readfirstlane_b32 s16, v200
	s_cmp_lt_i32 s16, s20
	s_cbranch_scc1 .Lp16_skip
	s_cmp_ge_i32 s16, s21
	s_cbranch_scc1 .Lp16_skip
	v_lshlrev_b32_e32 v0, 2, v16
	v_lshlrev_b32_e32 v1, 2, v18
	v_add_u32_e32 v0, s1, v0
	v_add_u32_e32 v1, s1, v1
	ds_read_b32 v16, v0 offset:32
	ds_read_b32 v18, v1 offset:32
	global_load_dwordx2 v[48:49], v[34:35], off offset:-2048
	global_load_dwordx2 v[50:51], v[34:35], off offset:-1536
	global_load_dwordx2 v[52:53], v[34:35], off offset:-1024
	global_load_dwordx4 v[0:3], v28, s[8:9]
	global_load_dwordx2 v[54:55], v[34:35], off offset:-512
	global_load_dwordx4 v[8:11], v64, s[8:9]
	global_load_dwordx4 v[4:7], v65, s[8:9]
	global_load_dwordx4 v[12:15], v66, s[8:9]
	global_load_dwordx2 v[56:57], v[34:35], off
	global_load_dwordx4 v[20:23], v36, s[8:9]
	global_load_dwordx4 v[24:27], v38, s[8:9]
	global_load_dwordx2 v[76:77], v[34:35], off offset:512
	global_load_dwordx2 v[78:79], v[34:35], off offset:1024
	global_load_dwordx2 v[80:81], v[34:35], off offset:1536
	global_load_dwordx4 v[68:71], v40, s[8:9]
	global_load_dwordx4 v[72:75], v42, s[8:9]
	v_lshl_add_u64 v[34:35], v[34:35], 0, s[6:7]
	s_waitcnt lgkmcnt(0)
	v_lshlrev_b32_e32 v16, 8, v16
	v_lshlrev_b32_e32 v18, 8, v18
	v_add_u32_e32 v16, v16, v17
	v_add_u32_e32 v18, v18, v19
	v_ashrrev_i32_e32 v17, 31, v16
	v_ashrrev_i32_e32 v19, 31, v18
	v_lshlrev_b64 v[16:17], 12, v[16:17]
	v_lshlrev_b64 v[18:19], 12, v[18:19]
	v_lshl_add_u64 v[16:17], v[30:31], 0, v[16:17]
	v_lshl_add_u64 v[18:19], v[30:31], 0, v[18:19]
	global_load_dwordx2 v[84:85], v[16:17], off
	global_load_dwordx2 v[86:87], v[18:19], off
	global_load_dwordx2 v[88:89], v[16:17], off offset:512
	global_load_dwordx2 v[90:91], v[18:19], off offset:512
	global_load_dwordx2 v[92:93], v[16:17], off offset:1024
	global_load_dwordx2 v[94:95], v[18:19], off offset:1024
	global_load_dwordx2 v[96:97], v[16:17], off offset:1536
	global_load_dwordx2 v[98:99], v[18:19], off offset:1536
	global_load_dwordx2 v[100:101], v[16:17], off offset:2048
	global_load_dwordx2 v[102:103], v[18:19], off offset:2048
	global_load_dwordx2 v[104:105], v[16:17], off offset:2560
	global_load_dwordx2 v[106:107], v[16:17], off offset:3072
	global_load_dwordx2 v[108:109], v[16:17], off offset:3584
	global_load_dwordx2 v[110:111], v[18:19], off offset:2560
	global_load_dwordx2 v[112:113], v[18:19], off offset:3072
	global_load_dwordx2 v[114:115], v[18:19], off offset:3584
	global_load_dwordx4 v[194:197], v29, s[14:15]
	global_load_dwordx2 v[198:199], v29, s[14:15] offset:16
	s_waitcnt vmcnt(2)
	v_lshlrev_b32_e32 v116, 16, v48
	v_and_b32_e32 v117, 0xffff0000, v48
	v_lshlrev_b32_e32 v48, 16, v49
	v_and_b32_e32 v49, 0xffff0000, v49
	v_lshlrev_b32_e32 v118, 16, v50
	v_and_b32_e32 v119, 0xffff0000, v50
	v_lshlrev_b32_e32 v50, 16, v51
	v_and_b32_e32 v51, 0xffff0000, v51
	v_lshlrev_b32_e32 v120, 16, v52
	v_and_b32_e32 v121, 0xffff0000, v52
	v_lshlrev_b32_e32 v52, 16, v53
	v_and_b32_e32 v53, 0xffff0000, v53
	v_lshlrev_b32_e32 v124, 16, v56
	v_and_b32_e32 v125, 0xffff0000, v56
	v_lshlrev_b32_e32 v132, 16, v86
	v_and_b32_e32 v133, 0xffff0000, v86
	v_lshlrev_b32_e32 v86, 16, v87
	v_and_b32_e32 v87, 0xffff0000, v87
	v_lshlrev_b32_e32 v136, 16, v90
	v_and_b32_e32 v137, 0xffff0000, v90
	v_lshlrev_b32_e32 v90, 16, v91
	v_and_b32_e32 v91, 0xffff0000, v91
	v_lshlrev_b32_e32 v82, 16, v84
	v_and_b32_e32 v83, 0xffff0000, v84
	v_lshlrev_b32_e32 v84, 16, v85
	v_and_b32_e32 v85, 0xffff0000, v85
	v_lshlrev_b32_e32 v134, 16, v88
	v_and_b32_e32 v135, 0xffff0000, v88
	v_lshlrev_b32_e32 v88, 16, v89
	v_and_b32_e32 v89, 0xffff0000, v89
	v_lshlrev_b32_e32 v140, 16, v94
	v_and_b32_e32 v141, 0xffff0000, v94
	v_lshlrev_b32_e32 v94, 16, v95
	v_and_b32_e32 v95, 0xffff0000, v95
	v_lshlrev_b32_e32 v148, 16, v102
	v_and_b32_e32 v149, 0xffff0000, v102
	v_lshlrev_b32_e32 v102, 16, v103
	v_and_b32_e32 v103, 0xffff0000, v103
	v_lshlrev_b32_e32 v156, 16, v112
	v_and_b32_e32 v157, 0xffff0000, v112
	v_lshlrev_b32_e32 v112, 16, v113
	v_and_b32_e32 v113, 0xffff0000, v113
	v_pk_mul_f32 v[86:87], v[46:47], v[86:87] op_sel:[1,0]
	v_pk_mul_f32 v[132:133], v[46:47], v[132:133] op_sel:[1,0]
	v_pk_mul_f32 v[90:91], v[46:47], v[90:91] op_sel:[1,0]
	v_pk_mul_f32 v[136:137], v[46:47], v[136:137] op_sel:[1,0]
	v_lshlrev_b32_e32 v138, 16, v92
	v_and_b32_e32 v139, 0xffff0000, v92
	v_lshlrev_b32_e32 v92, 16, v93
	v_and_b32_e32 v93, 0xffff0000, v93
	v_lshlrev_b32_e32 v144, 16, v98
	v_and_b32_e32 v145, 0xffff0000, v98
	v_lshlrev_b32_e32 v98, 16, v99
	v_and_b32_e32 v99, 0xffff0000, v99
	v_lshlrev_b32_e32 v146, 16, v100
	v_and_b32_e32 v147, 0xffff0000, v100
	v_lshlrev_b32_e32 v100, 16, v101
	v_and_b32_e32 v101, 0xffff0000, v101
	v_lshlrev_b32_e32 v152, 16, v110
	v_and_b32_e32 v153, 0xffff0000, v110
	v_lshlrev_b32_e32 v110, 16, v111
	v_and_b32_e32 v111, 0xffff0000, v111
	v_lshlrev_b32_e32 v154, 16, v106
	v_and_b32_e32 v155, 0xffff0000, v106
	v_lshlrev_b32_e32 v106, 16, v107
	v_and_b32_e32 v107, 0xffff0000, v107
	v_lshlrev_b32_e32 v160, 16, v114
	v_and_b32_e32 v161, 0xffff0000, v114
	v_lshlrev_b32_e32 v114, 16, v115
; __device__ __forceinline__ float bf_lo(unsigned w) { return __uint_as_float(w << 16); }
; __device__ __forceinline__ float bf_hi(unsigned w) { return __uint_as_float(w & 0xffff0000u); }
; __device__ __forceinline__ f32x4 ld4_bf(const bf16_t* p) { const u32x2 w = *(const u32x2*)p; return (f32x4){bf_lo(w.x), bf_hi(w.x), bf_lo(w.y), bf_hi(w.y)}; }
; __device__ __forceinline__ float sq4(const f32x4 v) { return (v[0] * v[0] + v[1] * v[1]) + (v[2] * v[2] + v[3] * v[3]); }
; __device__ __forceinline__ void phase_final(const Ctx& P, volatile LAS int* tab, int vcu, int G) {
;     ...
;         f32x4 v[8]; float ss = 0.f;
; #pragma unroll
;         for (int j = 0; j < 8; ++j) { const int c = 4 * lane + 256 * j; const f32x4 x4 = ld4_bf(xr + c), g4 = *(const f32x4*)(g2 + c); const u32x2 a = *(const u32x2*)(y1 + c), b = *(const u32x2*)(y2 + c);
;             const f32x4 ya = (f32x4){bf_lo(a.x), bf_hi(a.x), bf_lo(a.y), bf_hi(a.y)}, yb = (f32x4){bf_lo(b.x), bf_hi(b.x), bf_lo(b.y), bf_hi(b.y)};
;             v[j] = x4 + g4 * (ya * p1 + yb * p2); ss += sq4(v[j]); }
;         ss = wave_sum(ss); const float rstd = __builtin_amdgcn_rsqf(ss * (1.0f / DM) + EPS);
	v_and_b32_e32 v115, 0xffff0000, v115
	v_pk_mul_f32 v[140:141], v[46:47], v[140:141] op_sel:[1,0]
	v_pk_mul_f32 v[94:95], v[46:47], v[94:95] op_sel:[1,0]
	v_pk_mul_f32 v[102:103], v[46:47], v[102:103] op_sel:[1,0]
	v_pk_mul_f32 v[112:113], v[46:47], v[112:113] op_sel:[1,0]
	v_pk_fma_f32 v[82:83], v[46:47], v[82:83], v[132:133] op_sel_hi:[0,1,1]
	v_pk_fma_f32 v[84:85], v[46:47], v[84:85], v[86:87] op_sel_hi:[0,1,1]
	v_pk_fma_f32 v[86:87], v[46:47], v[134:135], v[136:137] op_sel_hi:[0,1,1]
	v_pk_fma_f32 v[88:89], v[46:47], v[88:89], v[90:91] op_sel_hi:[0,1,1]
	v_lshlrev_b32_e32 v56, 16, v57
	v_and_b32_e32 v57, 0xffff0000, v57
	v_lshlrev_b32_e32 v128, 16, v78
	v_and_b32_e32 v129, 0xffff0000, v78
	v_lshlrev_b32_e32 v78, 16, v79
	v_and_b32_e32 v79, 0xffff0000, v79
	v_lshlrev_b32_e32 v142, 16, v96
	v_and_b32_e32 v143, 0xffff0000, v96
	v_lshlrev_b32_e32 v96, 16, v97
	v_and_b32_e32 v97, 0xffff0000, v97
	v_lshlrev_b32_e32 v150, 16, v104
	v_and_b32_e32 v151, 0xffff0000, v104
	v_lshlrev_b32_e32 v104, 16, v105
	v_and_b32_e32 v105, 0xffff0000, v105
	v_lshlrev_b32_e32 v158, 16, v108
	v_and_b32_e32 v159, 0xffff0000, v108
	v_lshlrev_b32_e32 v108, 16, v109
	v_and_b32_e32 v109, 0xffff0000, v109
	v_pk_mul_f32 v[98:99], v[46:47], v[98:99] op_sel:[1,0]
	v_pk_mul_f32 v[144:145], v[46:47], v[144:145] op_sel:[1,0]
	v_pk_mul_f32 v[148:149], v[46:47], v[148:149] op_sel:[1,0]
	v_pk_mul_f32 v[152:153], v[46:47], v[152:153] op_sel:[1,0]
	v_pk_mul_f32 v[110:111], v[46:47], v[110:111] op_sel:[1,0]
	v_pk_mul_f32 v[156:157], v[46:47], v[156:157] op_sel:[1,0]
	v_pk_mul_f32 v[114:115], v[46:47], v[114:115] op_sel:[1,0]
	v_pk_mul_f32 v[160:161], v[46:47], v[160:161] op_sel:[1,0]
	v_pk_fma_f32 v[90:91], v[46:47], v[92:93], v[94:95] op_sel_hi:[0,1,1]
	v_pk_fma_f32 v[92:93], v[46:47], v[138:139], v[140:141] op_sel_hi:[0,1,1]
	v_pk_fma_f32 v[100:101], v[46:47], v[100:101], v[102:103] op_sel_hi:[0,1,1]
	v_pk_fma_f32 v[106:107], v[46:47], v[106:107], v[112:113] op_sel_hi:[0,1,1]
	v_pk_fma_f32 v[2:3], v[2:3], v[84:85], v[48:49]
	v_pk_fma_f32 v[0:1], v[0:1], v[82:83], v[116:117]
	v_pk_fma_f32 v[10:11], v[10:11], v[88:89], v[50:51]
	v_pk_fma_f32 v[8:9], v[8:9], v[86:87], v[118:119]
	v_lshlrev_b32_e32 v122, 16, v54
	v_and_b32_e32 v123, 0xffff0000, v54
	v_lshlrev_b32_e32 v54, 16, v55
	v_and_b32_e32 v55, 0xffff0000, v55
	v_lshlrev_b32_e32 v130, 16, v80
	v_and_b32_e32 v131, 0xffff0000, v80
	v_lshlrev_b32_e32 v80, 16, v81
	v_and_b32_e32 v81, 0xffff0000, v81
	v_pk_fma_f32 v[94:95], v[46:47], v[142:143], v[144:145] op_sel_hi:[0,1,1]
	v_pk_fma_f32 v[96:97], v[46:47], v[96:97], v[98:99] op_sel_hi:[0,1,1]
	v_pk_fma_f32 v[98:99], v[46:47], v[146:147], v[148:149] op_sel_hi:[0,1,1]
	v_pk_fma_f32 v[102:103], v[46:47], v[104:105], v[110:111] op_sel_hi:[0,1,1]
	v_pk_fma_f32 v[104:105], v[46:47], v[150:151], v[152:153] op_sel_hi:[0,1,1]
	v_pk_fma_f32 v[110:111], v[46:47], v[154:155], v[156:157] op_sel_hi:[0,1,1]
	v_pk_fma_f32 v[112:113], v[46:47], v[158:159], v[160:161] op_sel_hi:[0,1,1]
	v_pk_fma_f32 v[46:47], v[46:47], v[108:109], v[114:115] op_sel_hi:[0,1,1]
	v_pk_fma_f32 v[4:5], v[4:5], v[92:93], v[120:121]
	v_pk_fma_f32 v[6:7], v[6:7], v[90:91], v[52:53]
	v_pk_fma_f32 v[22:23], v[22:23], v[100:101], v[56:57]
	v_pk_fma_f32 v[48:49], v[70:71], v[106:107], v[78:79]
	v_mov_b32_e32 v56, v1
	v_mov_b32_e32 v57, v9
	v_mov_b32_e32 v70, v3
	v_mov_b32_e32 v71, v11
	v_pk_fma_f32 v[14:15], v[14:15], v[96:97], v[54:55]
	v_pk_fma_f32 v[50:51], v[68:69], v[110:111], v[128:129]
	v_pk_fma_f32 v[46:47], v[74:75], v[46:47], v[80:81]
	v_pk_fma_f32 v[52:53], v[72:73], v[112:113], v[130:131]
	v_mov_b32_e32 v54, v0
	v_mov_b32_e32 v55, v8
	v_mov_b32_e32 v68, v2
	v_mov_b32_e32 v69, v10
	v_pk_mul_f32 v[72:73], v[6:7], v[6:7]
	v_pk_mul_f32 v[74:75], v[4:5], v[4:5]
	v_pk_mul_f32 v[56:57], v[56:57], v[56:57]
	v_pk_mul_f32 v[70:71], v[70:71], v[70:71]
	v_lshlrev_b32_e32 v126, 16, v76
	v_and_b32_e32 v127, 0xffff0000, v76
	v_lshlrev_b32_e32 v76, 16, v77
	v_and_b32_e32 v77, 0xffff0000, v77
	v_pk_fma_f32 v[12:13], v[12:13], v[94:95], v[122:123]
	v_pk_mov_b32 v[88:89], v[74:75], v[72:73] op_sel:[1,0]
	v_mov_b32_e32 v75, v73
	v_pk_fma_f32 v[54:55], v[54:55], v[54:55], v[56:57]
	v_pk_fma_f32 v[56:57], v[68:69], v[68:69], v[70:71]
	v_pk_fma_f32 v[20:21], v[20:21], v[98:99], v[124:125]
	v_pk_fma_f32 v[26:27], v[26:27], v[102:103], v[76:77]
	v_mul_f32_e32 v76, v13, v13
	v_mul_f32_e32 v78, v15, v15
	v_pk_add_f32 v[68:69], v[88:89], v[74:75]
	v_pk_add_f32 v[54:55], v[54:55], v[56:57]
	v_pk_fma_f32 v[24:25], v[24:25], v[104:105], v[126:127]
	v_mul_f32_e32 v87, v20, v20
	v_mul_f32_e32 v90, v21, v21
	v_mul_f32_e32 v91, v22, v22
	v_mul_f32_e32 v92, v23, v23
	v_pk_fma_f32 v[72:73], v[12:13], v[12:13], v[76:77] op_sel_hi:[1,1,0]
	v_pk_fma_f32 v[76:77], v[14:15], v[14:15], v[78:79] op_sel_hi:[1,1,0]
	v_pk_add_f32 v[56:57], v[68:69], v[68:69] op_sel:[0,1] op_sel_hi:[1,0]
	v_pk_add_f32 v[54:55], v[54:55], v[54:55] op_sel:[0,1] op_sel_hi:[1,0]
	v_pk_mul_f32 v[80:81], v[26:27], v[26:27]
	v_pk_mul_f32 v[82:83], v[24:25], v[24:25]
	v_mov_b32_e32 v73, v91
	v_mov_b32_e32 v77, v92
	v_mov_b32_e32 v57, v90
	v_mov_b32_e32 v55, v87
	v_pk_mov_b32 v[78:79], v[82:83], v[80:81] op_sel:[1,0]
	v_mov_b32_e32 v83, v81
	v_pk_add_f32 v[68:69], v[72:73], v[76:77]
	v_pk_add_f32 v[54:55], v[54:55], v[56:57]
	v_mul_f32_e32 v84, v51, v51
	v_mul_f32_e32 v86, v49, v49
	v_pk_add_f32 v[70:71], v[78:79], v[82:83]
	v_pk_add_f32 v[54:55], v[54:55], v[68:69]
	v_mul_f32_e32 v93, v52, v52
	v_mul_f32_e32 v94, v53, v53
	v_mul_f32_e32 v95, v46, v46
	v_mul_f32_e32 v96, v47, v47
	v_pk_fma_f32 v[80:81], v[50:51], v[50:51], v[84:85] op_sel_hi:[1,1,0]
	v_pk_fma_f32 v[84:85], v[48:49], v[48:49], v[86:87] op_sel_hi:[1,1,0]
	v_pk_add_f32 v[70:71], v[70:71], v[70:71] op_sel:[0,1] op_sel_hi:[1,0]
	v_pk_add_f32 v[54:55], v[54:55], v[54:55] op_sel:[0,1] op_sel_hi:[1,0]
	v_mov_b32_e32 v81, v95
	v_mov_b32_e32 v85, v96
	v_mov_b32_e32 v71, v94
	v_mov_b32_e32 v55, v93
	v_pk_add_f32 v[72:73], v[80:81], v[84:85]
	v_pk_add_f32 v[54:55], v[54:55], v[70:71]
	s_nop 0
	v_pk_add_f32 v[54:55], v[54:55], v[72:73]
	s_nop 0
	v_add_f32_e32 v54, v54, v55
	ds_bpermute_b32 v55, v58, v54
	s_waitcnt lgkmcnt(0)
; __device__ __forceinline__ void phase_final(const Ctx& P, volatile LAS int* tab, int vcu, int G) {
;     ...
;         ss = wave_sum(ss); const float rstd = __builtin_amdgcn_rsqf(ss * (1.0f / DM) + EPS);
; #pragma unroll
;         for (int j = 0; j < 8; ++j) { const int c = 4 * lane + 256 * j; const f32x4 fg = *(const f32x4*)(P.in[34] + c); *(f32x4*)(P.out + (size_t)row * DM + c) = v[j] * rstd * fg; }
;     }
	v_add_f32_e32 v54, v54, v55
	ds_bpermute_b32 v55, v59, v54
	s_waitcnt lgkmcnt(0)
	v_add_f32_e32 v54, v54, v55
	ds_bpermute_b32 v55, v60, v54
	s_waitcnt lgkmcnt(0)
	v_add_f32_e32 v54, v54, v55
	ds_bpermute_b32 v55, v61, v54
	s_waitcnt lgkmcnt(0)
	v_add_f32_e32 v54, v54, v55
	ds_bpermute_b32 v55, v62, v54
	s_waitcnt lgkmcnt(0)
	v_add_f32_e32 v54, v54, v55
	ds_bpermute_b32 v55, v63, v54
	s_waitcnt lgkmcnt(0)
	v_add_f32_e32 v54, v54, v55
	v_fmamk_f32 v54, v54, 0x3a000000, v67
	v_rsq_f32_e32 v54, v54
	s_nop 0
	v_pk_mul_f32 v[0:1], v[0:1], v[54:55] op_sel_hi:[1,0]
	v_pk_mul_f32 v[2:3], v[2:3], v[54:55] op_sel_hi:[1,0]
	v_pk_mul_f32 v[8:9], v[8:9], v[54:55] op_sel_hi:[1,0]
	v_pk_mul_f32 v[10:11], v[10:11], v[54:55] op_sel_hi:[1,0]
	v_pk_mul_f32 v[4:5], v[4:5], v[54:55] op_sel_hi:[1,0]
	v_pk_mul_f32 v[6:7], v[6:7], v[54:55] op_sel_hi:[1,0]
	v_pk_mul_f32 v[12:13], v[12:13], v[54:55] op_sel_hi:[1,0]
	v_pk_mul_f32 v[14:15], v[14:15], v[54:55] op_sel_hi:[1,0]
	v_pk_mul_f32 v[20:21], v[20:21], v[54:55] op_sel_hi:[1,0]
	v_pk_mul_f32 v[22:23], v[22:23], v[54:55] op_sel_hi:[1,0]
	v_pk_mul_f32 v[24:25], v[24:25], v[54:55] op_sel_hi:[1,0]
	v_pk_mul_f32 v[26:27], v[26:27], v[54:55] op_sel_hi:[1,0]
	v_pk_mul_f32 v[68:69], v[50:51], v[54:55] op_sel_hi:[1,0]
	v_pk_mul_f32 v[70:71], v[48:49], v[54:55] op_sel_hi:[1,0]
	v_pk_mul_f32 v[72:73], v[52:53], v[54:55] op_sel_hi:[1,0]
	v_pk_mul_f32 v[74:75], v[46:47], v[54:55] op_sel_hi:[1,0]
	v_pk_mul_f32 v[0:1], v[162:163], v[0:1]
	v_pk_mul_f32 v[2:3], v[164:165], v[2:3]
	global_store_dwordx4 v[32:33], v[0:3], off offset:-4096
	v_pk_mul_f32 v[8:9], v[166:167], v[8:9]
	v_pk_mul_f32 v[10:11], v[168:169], v[10:11]
	global_store_dwordx4 v[32:33], v[8:11], off offset:-3072
	v_pk_mul_f32 v[4:5], v[170:171], v[4:5]
	v_pk_mul_f32 v[6:7], v[172:173], v[6:7]
	global_store_dwordx4 v[32:33], v[4:7], off offset:-2048
	v_pk_mul_f32 v[12:13], v[174:175], v[12:13]
	v_pk_mul_f32 v[14:15], v[176:177], v[14:15]
	global_store_dwordx4 v[32:33], v[12:15], off offset:-1024
	v_pk_mul_f32 v[20:21], v[178:179], v[20:21]
	v_pk_mul_f32 v[22:23], v[180:181], v[22:23]
	global_store_dwordx4 v[32:33], v[20:23], off
	v_pk_mul_f32 v[24:25], v[182:183], v[24:25]
	v_pk_mul_f32 v[26:27], v[184:185], v[26:27]
	global_store_dwordx4 v[32:33], v[24:27], off offset:1024
	v_pk_mul_f32 v[68:69], v[186:187], v[68:69]
	v_pk_mul_f32 v[70:71], v[188:189], v[70:71]
	global_store_dwordx4 v[32:33], v[68:71], off offset:2048
	v_pk_mul_f32 v[72:73], v[190:191], v[72:73]
	v_pk_mul_f32 v[74:75], v[192:193], v[74:75]
	global_store_dwordx4 v[32:33], v[72:75], off offset:3072
	v_lshl_add_u64 v[32:33], v[32:33], 0, s[4:5]
	s_waitcnt vmcnt(8)
	s_cmp_lg_u32 s17, 0
	s_cbranch_scc1 .LBB0_2712
	s_branch .LBB0_2713
.Lp16_skip:
	global_load_dwordx4 v[194:197], v29, s[14:15]
	global_load_dwordx2 v[198:199], v29, s[14:15] offset:16
	v_lshl_add_u64 v[34:35], v[34:35], 0, s[6:7]
	v_lshl_add_u64 v[32:33], v[32:33], 0, s[4:5]
	s_waitcnt vmcnt(0)
	s_cmp_lg_u32 s17, 0
	s_cbranch_scc1 .LBB0_2712
.LBB0_2713:
	s_cmp_eq_u32 s99, 2
	s_cbranch_scc1 .Lp16a_done
	s_endpgm
.Lp16a_done:
	s_mov_b32 s99, 3
	s_mov_b64 s[0:1], s[90:91]
	v_mov_b32_e32 v0, v203
	s_waitcnt vmcnt(0) lgkmcnt(0)
	s_branch .Lseam15
